# conv1r plus conversion quota per workgroup in the attention phase 7 -> 3 claims (balance the two halves)
# speedup vs baseline: 1.0152x; 1.0152x over previous
; __device__ __forceinline__ unsigned xb_ld(unsigned* p)              { return __hip_atomic_load(p, __ATOMIC_RELAXED, __HIP_MEMORY_SCOPE_AGENT); }
; __device__ __forceinline__ unsigned xb_add(unsigned* p, unsigned v) { return __hip_atomic_fetch_add(p, v, __ATOMIC_RELAXED, __HIP_MEMORY_SCOPE_AGENT); }
;     ...
;     unsigned ahead = 0xFFFFFFFFu;
;     if (tl == 0 && max_claims > 0) { if (xb_ld(qw) < (unsigned)target) ahead = xb_add(qw, 32u); }
;     for (int nc = 0; nc < max_claims; ++nc) {
;         if (tl == 0) { st[6] = ahead; if (ahead < (unsigned)target && nc + 1 < max_claims) ahead = (ahead + 32u < (unsigned)target) ? xb_add(qw, 32u) : 0xFFFFFFFFu; }
;         __syncthreads();
;         const unsigned base = st[6];
.LBB0_698:
	s_and_saveexec_b64 s[0:1], s[2:3]
	s_cbranch_execz .LBB0_706
	v_readlane_b32 s14, v254, 27
	s_cmp_lt_u32 s30, 2
	v_cmp_gt_u32_e32 vcc, s25, v129
	v_mov_b32_e32 v139, s14
	s_cselect_b64 s[14:15], -1, 0
	s_and_b64 s[16:17], vcc, s[14:15]
	ds_write_b32 v139, v129
	s_and_saveexec_b64 s[14:15], s[16:17]
	s_cbranch_execz .LBB0_705
	v_cmp_gt_u32_e32 vcc, s27, v129
	v_mov_b32_e32 v129, -1
	s_and_saveexec_b64 s[16:17], vcc
	s_cbranch_execz .LBB0_704
	s_mov_b64 s[20:21], exec
	v_mbcnt_lo_u32_b32 v129, s20, 0
	v_mbcnt_hi_u32_b32 v129, s21, v129
	v_cmp_eq_u32_e32 vcc, 0, v129
	s_and_saveexec_b64 s[18:19], vcc
	s_cbranch_execz .LBB0_703
	s_bcnt1_i32_b64 s20, s[20:21]
	s_lshl_b32 s20, s20, 5
	v_mov_b32_e32 v139, s20
	global_atomic_add v139, v193, v139, s[4:5] sc0

; __device__ __forceinline__ unsigned xb_add(unsigned* p, unsigned v) { return __hip_atomic_fetch_add(p, v, __ATOMIC_RELAXED, __HIP_MEMORY_SCOPE_AGENT); }
;     __device__ __forceinline__ unsigned char* ws() const { return *(unsigned char* const __attribute__((address_space(4)))*)(p + 232); }
;     ...
;     for (int nc = 0; nc < max_claims; ++nc) {
;         if (tl == 0) { st[6] = ahead; if (ahead < (unsigned)target && nc + 1 < max_claims) ahead = (ahead + 32u < (unsigned)target) ? xb_add(qw, 32u) : 0xFFFFFFFFu; }
;         __syncthreads();
;         const unsigned base = st[6];
;         if (base < (unsigned)Q_TOTAL) {
;             const int q0 = (int)base + wave; const bool v0 = q0 < Q_TOTAL, v1 = q0 + 8 < Q_TOTAL, v2 = q0 + 16 < Q_TOTAL, v3 = q0 + 24 < Q_TOTAL;
;             float ta[64], tb[64]; CvtDesc da, db;
;             if (v0) { da = conv_expert_desc(a, ws, q0); cvt_load(da, ta, lane); }
;             if (v1) { db = conv_expert_desc(a, ws, q0 + 8); cvt_load(db, tb, lane); }
;             if (v0) cvt_finish(da, ta, scr, lane);
;             if (v2) { da = conv_expert_desc(a, ws, q0 + 16); cvt_load(da, ta, lane); }
;             if (v1) cvt_finish(db, tb, scr, lane);
;             if (v3) { db = conv_expert_desc(a, ws, q0 + 24); cvt_load(db, tb, lane); }
;             if (v2) cvt_finish(da, ta, scr, lane);
;             if (v3) cvt_finish(db, tb, scr, lane);
;         }
;         if (base >= (unsigned)target) break;
;         __syncthreads();
;     }
.LBB0_779:
	s_cmp_ge_u32 s35, s25
	s_mov_b64 s[0:1], -1
	s_cbranch_scc1 .LBB0_697
	s_add_i32 s30, s30, 1
	s_cmp_eq_u32 s30, 3
	s_cselect_b64 s[0:1], -1, 0
	s_barrier
	s_branch .LBB0_697
